# v10 (peeled K-loops) + int8 phases: from the second unit on the peeled iteration skips its first two vmcnt waits (they only drained the previous epilogue's result stores)
# speedup vs baseline: 1.0132x; 1.0001x over previous
.LBB0_234:
	s_mov_b32 s100, 0
	v_readlane_b32 s2, v250, 40
	v_readlane_b32 s3, v250, 41
	s_cmp_lt_i32 s2, 3
	s_cselect_b64 s[2:3], -1, 0
	s_add_u32 s72, s78, 0x32500000
	s_addc_u32 s73, s79, 0
	s_and_b64 s[0:1], s[2:3], s[0:1]
	s_andn2_b64 vcc, exec, s[0:1]
	s_cbranch_vccnz .LBB0_285
	s_cmp_eq_u32 s97, 0x100
	s_cselect_b32 s98, 184, s97
	v_readfirstlane_b32 s30, v0
	s_lshr_b32 s30, s30, 6
	s_cmp_eq_u32 s97, 0x100
	s_cbranch_scc0 .Lq2_all
	s_cmpk_lt_i32 s74, 184
	s_cbranch_scc1 .Lq2_gemm
	s_sub_u32 s12, s74, 184
	s_lshl_b32 s12, s12, 3
	s_add_u32 s12, s12, s30
	s_add_u32 s12, s12, 0x3000
	s_movk_i32 s13, 576
	s_mov_b32 s14, 0x5328
	s_mov_b32 s46, 2
	s_branch .Lq_conv

.LBB0_243:
	s_ashr_i32 s17, s16, 31
	s_lshl_b64 s[18:19], s[16:17], 19
	s_add_u32 s18, s72, s18
	s_addc_u32 s19, s73, s19
	s_and_b64 s[20:21], s[0:1], exec
	s_cselect_b32 s17, s19, s25
	s_cselect_b32 s47, s18, s24
	s_ashr_i32 s15, s14, 31
	s_lshl_b64 s[20:21], s[14:15], 19
	s_add_u32 s20, s30, s20
	s_addc_u32 s21, s31, s21
	s_and_b64 s[28:29], s[0:1], exec
	s_cselect_b32 s15, s21, s27
	s_cselect_b32 s48, s20, s26
	s_add_u32 s24, s24, 0x40080
	s_addc_u32 s25, s25, 0
	s_add_u32 s49, s26, 0x100
	v_mov_b32_e32 v2, 0
	s_addc_u32 s50, s27, 0
	s_mov_b32 s51, -2
	ds_read_b128 v[158:161], v192
	ds_read_b128 v[154:157], v192 offset:1024
	ds_read_b128 v[150:153], v192 offset:2048
	ds_read_b128 v[146:149], v192 offset:3072
	ds_read_b128 v[142:145], v193
	ds_read_b128 v[138:141], v193 offset:1024
	ds_read_b128 v[134:137], v193 offset:2048
	ds_read_b128 v[130:133], v193 offset:3072
	s_add_u32 s26, s24, 0xfffc0080
	s_addc_u32 s27, s25, -1
	s_cmp_eq_u32 s51, 12
	s_cselect_b32 s29, s17, s27
	s_cselect_b32 s28, s47, s26
	s_cselect_b32 s27, s15, s50
	s_cselect_b32 s26, s48, s49
	v_lshl_add_u64 v[222:223], s[24:25], 0, v[170:171]
	s_add_i32 m0, s23, 0xc000
	ds_read_b128 v[182:185], v194
	ds_read_b128 v[186:189], v194 offset:1024
	ds_read_b128 v[198:201], v194 offset:2048
	ds_read_b128 v[202:205], v194 offset:3072
	ds_read_b128 v[206:209], v194 offset:4096
	ds_read_b128 v[210:213], v194 offset:5120
	ds_read_b128 v[214:217], v194 offset:6144
	ds_read_b128 v[218:221], v194 offset:7168
	global_load_lds_dwordx4 v[222:223], off
	v_lshl_add_u64 v[222:223], s[24:25], 0, v[172:173]
	s_add_i32 m0, s23, 0xe000
	s_nop 0
	global_load_lds_dwordx4 v[222:223], off
	s_cmp_lg_u32 s100, 0
	s_cbranch_scc1 .Lpw_244_0
	s_waitcnt vmcnt(8)
.Lpw_244_0:
	s_waitcnt lgkmcnt(0)
	s_barrier
	s_setprio 1
	s_waitcnt lgkmcnt(0)
	v_mfma_i32_16x16x64_i8 v[126:129], v[158:161], v[182:185], 0
	s_nop 0
	v_mfma_i32_16x16x64_i8 v[126:129], v[154:157], v[186:189], v[126:129]
	v_mfma_i32_16x16x64_i8 v[122:125], v[150:153], v[182:185], 0
	s_nop 0
	v_mfma_i32_16x16x64_i8 v[122:125], v[146:149], v[186:189], v[122:125]
	v_mfma_i32_16x16x64_i8 v[118:121], v[158:161], v[198:201], 0
	s_nop 0
	v_mfma_i32_16x16x64_i8 v[118:121], v[154:157], v[202:205], v[118:121]
	v_mfma_i32_16x16x64_i8 v[114:117], v[150:153], v[198:201], 0
	s_nop 0
	v_mfma_i32_16x16x64_i8 v[114:117], v[146:149], v[202:205], v[114:117]
	v_mfma_i32_16x16x64_i8 v[98:101], v[158:161], v[206:209], 0
	s_nop 0
	v_mfma_i32_16x16x64_i8 v[98:101], v[154:157], v[210:213], v[98:101]
	v_mfma_i32_16x16x64_i8 v[94:97], v[150:153], v[206:209], 0
	s_nop 0
	v_mfma_i32_16x16x64_i8 v[94:97], v[146:149], v[210:213], v[94:97]
	v_mfma_i32_16x16x64_i8 v[86:89], v[158:161], v[214:217], 0
	s_nop 0
	v_mfma_i32_16x16x64_i8 v[86:89], v[154:157], v[218:221], v[86:89]
	v_mfma_i32_16x16x64_i8 v[78:81], v[150:153], v[214:217], 0
	s_nop 0
	v_mfma_i32_16x16x64_i8 v[78:81], v[146:149], v[218:221], v[78:81]
	s_setprio 0
	s_setprio 1
	v_mfma_i32_16x16x64_i8 v[110:113], v[142:145], v[182:185], 0
	s_nop 0
	v_mfma_i32_16x16x64_i8 v[110:113], v[138:141], v[186:189], v[110:113]
	v_mfma_i32_16x16x64_i8 v[106:109], v[134:137], v[182:185], 0
	s_nop 0
	v_mfma_i32_16x16x64_i8 v[106:109], v[130:133], v[186:189], v[106:109]
	v_mfma_i32_16x16x64_i8 v[102:105], v[142:145], v[198:201], 0
	s_nop 0
	v_mfma_i32_16x16x64_i8 v[102:105], v[138:141], v[202:205], v[102:105]
	v_mfma_i32_16x16x64_i8 v[90:93], v[134:137], v[198:201], 0
	s_nop 0
	v_mfma_i32_16x16x64_i8 v[90:93], v[130:133], v[202:205], v[90:93]
	v_mfma_i32_16x16x64_i8 v[82:85], v[142:145], v[206:209], 0
	s_nop 0
	v_mfma_i32_16x16x64_i8 v[82:85], v[138:141], v[210:213], v[82:85]
	v_mfma_i32_16x16x64_i8 v[74:77], v[134:137], v[206:209], 0
	s_nop 0
	v_mfma_i32_16x16x64_i8 v[74:77], v[130:133], v[210:213], v[74:77]
	v_mfma_i32_16x16x64_i8 v[70:73], v[142:145], v[214:217], 0
	s_nop 0
	v_mfma_i32_16x16x64_i8 v[70:73], v[138:141], v[218:221], v[70:73]
	v_mfma_i32_16x16x64_i8 v[66:69], v[134:137], v[214:217], 0
	s_nop 0
	v_mfma_i32_16x16x64_i8 v[66:69], v[130:133], v[218:221], v[66:69]
	s_setprio 0
	s_barrier
	s_add_i32 s52, s43, s33
	v_lshl_add_u64 v[182:183], s[26:27], 0, v[166:167]
	s_mov_b32 m0, s52
	ds_read_b128 v[198:201], v194 offset:16384
	ds_read_b128 v[202:205], v194 offset:17408
	ds_read_b128 v[206:209], v194 offset:18432
	ds_read_b128 v[210:213], v194 offset:19456
	ds_read_b128 v[214:217], v194 offset:20480
	ds_read_b128 v[218:221], v194 offset:21504
	ds_read_b128 v[222:225], v194 offset:22528
	ds_read_b128 v[226:229], v194 offset:23552
	global_load_lds_dwordx4 v[182:183], off
	s_add_i32 m0, s52, 0x2000
	s_add_u32 s52, s26, 0x40000
	v_lshl_add_u64 v[184:185], s[26:27], 0, v[162:163]
	s_addc_u32 s53, s27, 0
	s_add_i32 s54, s44, s33
	global_load_lds_dwordx4 v[184:185], off
	v_lshl_add_u64 v[186:187], s[52:53], 0, v[166:167]
	s_mov_b32 m0, s54
	v_lshl_add_u64 v[188:189], s[28:29], 0, v[164:165]
	global_load_lds_dwordx4 v[186:187], off
	v_lshl_add_u64 v[186:187], s[52:53], 0, v[162:163]
	s_add_i32 m0, s54, 0x2000
	s_nop 0
	global_load_lds_dwordx4 v[186:187], off
	v_lshl_add_u64 v[186:187], s[28:29], 0, v[168:169]
	s_mov_b32 m0, s23
	s_nop 0
	global_load_lds_dwordx4 v[186:187], off
	s_mov_b32 m0, s36
	s_nop 0
	global_load_lds_dwordx4 v[188:189], off
	s_cmp_lg_u32 s100, 0
	s_cbranch_scc1 .Lpw_244_1
	s_waitcnt vmcnt(8)
.Lpw_244_1:
	s_add_u32 s100, s100, 1
	s_waitcnt lgkmcnt(0)
	s_barrier
	s_setprio 1
	s_waitcnt lgkmcnt(0)
	v_mfma_i32_16x16x64_i8 v[62:65], v[158:161], v[198:201], 0
	s_nop 0
	v_mfma_i32_16x16x64_i8 v[62:65], v[154:157], v[202:205], v[62:65]
	v_mfma_i32_16x16x64_i8 v[58:61], v[150:153], v[198:201], 0
	s_nop 0
	v_mfma_i32_16x16x64_i8 v[58:61], v[146:149], v[202:205], v[58:61]
	v_mfma_i32_16x16x64_i8 v[54:57], v[158:161], v[206:209], 0
	s_nop 0
	v_mfma_i32_16x16x64_i8 v[54:57], v[154:157], v[210:213], v[54:57]
	v_mfma_i32_16x16x64_i8 v[46:49], v[150:153], v[206:209], 0
	s_nop 0
	v_mfma_i32_16x16x64_i8 v[46:49], v[146:149], v[210:213], v[46:49]
	v_mfma_i32_16x16x64_i8 v[38:41], v[158:161], v[214:217], 0
	s_nop 0
	v_mfma_i32_16x16x64_i8 v[38:41], v[154:157], v[218:221], v[38:41]
	v_mfma_i32_16x16x64_i8 v[30:33], v[150:153], v[214:217], 0
	s_nop 0
	v_mfma_i32_16x16x64_i8 v[30:33], v[146:149], v[218:221], v[30:33]
	v_mfma_i32_16x16x64_i8 v[22:25], v[158:161], v[222:225], 0
	s_nop 0
	v_mfma_i32_16x16x64_i8 v[22:25], v[154:157], v[226:229], v[22:25]
	v_mfma_i32_16x16x64_i8 v[14:17], v[150:153], v[222:225], 0
	s_nop 0
	v_mfma_i32_16x16x64_i8 v[14:17], v[146:149], v[226:229], v[14:17]
	s_setprio 0
	s_setprio 1
	v_mfma_i32_16x16x64_i8 v[50:53], v[142:145], v[198:201], 0
	s_nop 0
	v_mfma_i32_16x16x64_i8 v[50:53], v[138:141], v[202:205], v[50:53]
	v_mfma_i32_16x16x64_i8 v[42:45], v[134:137], v[198:201], 0
	s_nop 0
	v_mfma_i32_16x16x64_i8 v[42:45], v[130:133], v[202:205], v[42:45]
	v_mfma_i32_16x16x64_i8 v[34:37], v[142:145], v[206:209], 0
	s_nop 0
	v_mfma_i32_16x16x64_i8 v[34:37], v[138:141], v[210:213], v[34:37]
	v_mfma_i32_16x16x64_i8 v[26:29], v[134:137], v[206:209], 0
	s_nop 0
	v_mfma_i32_16x16x64_i8 v[26:29], v[130:133], v[210:213], v[26:29]
	v_mfma_i32_16x16x64_i8 v[18:21], v[142:145], v[214:217], 0
	s_nop 0
	v_mfma_i32_16x16x64_i8 v[18:21], v[138:141], v[218:221], v[18:21]
	v_mfma_i32_16x16x64_i8 v[10:13], v[134:137], v[214:217], 0
	s_nop 0
	v_mfma_i32_16x16x64_i8 v[10:13], v[130:133], v[218:221], v[10:13]
	v_mfma_i32_16x16x64_i8 v[6:9], v[142:145], v[222:225], 0
	s_nop 0
	v_mfma_i32_16x16x64_i8 v[6:9], v[138:141], v[226:229], v[6:9]
	v_mfma_i32_16x16x64_i8 v[2:5], v[134:137], v[222:225], 0
	s_nop 0
	v_mfma_i32_16x16x64_i8 v[2:5], v[130:133], v[226:229], v[2:5]
	s_setprio 0
	s_barrier
	s_add_i32 s52, 0, 0x18000
	s_add_i32 s53, 0, 0x1c000
	v_add_u32_e32 v142, s52, v190
	v_add_u32_e32 v158, s53, v190
	ds_read_b128 v[130:133], v142
	ds_read_b128 v[134:137], v142 offset:1024
	ds_read_b128 v[138:141], v142 offset:2048
	ds_read_b128 v[142:145], v142 offset:3072
	ds_read_b128 v[146:149], v158
	ds_read_b128 v[150:153], v158 offset:1024
	ds_read_b128 v[154:157], v158 offset:2048
	ds_read_b128 v[158:161], v158 offset:3072
	s_add_u32 s28, s28, 0x40000
	s_addc_u32 s29, s29, 0
	s_mov_b32 m0, s37
	v_lshl_add_u64 v[230:231], s[28:29], 0, v[168:169]
	ds_read_b128 v[198:201], v194 offset:32768
	ds_read_b128 v[202:205], v194 offset:33792
	ds_read_b128 v[206:209], v194 offset:34816
	ds_read_b128 v[210:213], v194 offset:35840
	ds_read_b128 v[214:217], v194 offset:36864
	ds_read_b128 v[218:221], v194 offset:37888
	ds_read_b128 v[222:225], v194 offset:38912
	ds_read_b128 v[226:229], v194 offset:39936
	global_load_lds_dwordx4 v[230:231], off
	v_lshl_add_u64 v[230:231], s[28:29], 0, v[164:165]
	s_mov_b32 m0, s38
	s_nop 0
	global_load_lds_dwordx4 v[230:231], off
	s_waitcnt vmcnt(8)
	s_waitcnt lgkmcnt(0)
	s_barrier
	s_setprio 1
	s_waitcnt lgkmcnt(0)
	v_mfma_i32_16x16x64_i8 v[126:129], v[130:133], v[198:201], v[126:129]
	s_nop 0
	v_mfma_i32_16x16x64_i8 v[126:129], v[134:137], v[202:205], v[126:129]
	v_mfma_i32_16x16x64_i8 v[122:125], v[138:141], v[198:201], v[122:125]
	s_nop 0
	v_mfma_i32_16x16x64_i8 v[122:125], v[142:145], v[202:205], v[122:125]
	v_mfma_i32_16x16x64_i8 v[118:121], v[130:133], v[206:209], v[118:121]
	s_nop 0
	v_mfma_i32_16x16x64_i8 v[118:121], v[134:137], v[210:213], v[118:121]
	v_mfma_i32_16x16x64_i8 v[114:117], v[138:141], v[206:209], v[114:117]
	s_nop 0
	v_mfma_i32_16x16x64_i8 v[114:117], v[142:145], v[210:213], v[114:117]
	v_mfma_i32_16x16x64_i8 v[98:101], v[130:133], v[214:217], v[98:101]
	s_nop 0
	v_mfma_i32_16x16x64_i8 v[98:101], v[134:137], v[218:221], v[98:101]
	v_mfma_i32_16x16x64_i8 v[94:97], v[138:141], v[214:217], v[94:97]
	s_nop 0
	v_mfma_i32_16x16x64_i8 v[94:97], v[142:145], v[218:221], v[94:97]
	v_mfma_i32_16x16x64_i8 v[86:89], v[130:133], v[222:225], v[86:89]
	s_nop 0
	v_mfma_i32_16x16x64_i8 v[86:89], v[134:137], v[226:229], v[86:89]
	v_mfma_i32_16x16x64_i8 v[78:81], v[138:141], v[222:225], v[78:81]
	s_nop 0
	v_mfma_i32_16x16x64_i8 v[78:81], v[142:145], v[226:229], v[78:81]
	s_setprio 0
	s_setprio 1
	v_mfma_i32_16x16x64_i8 v[110:113], v[146:149], v[198:201], v[110:113]
	s_nop 0
	v_mfma_i32_16x16x64_i8 v[110:113], v[150:153], v[202:205], v[110:113]
	v_mfma_i32_16x16x64_i8 v[106:109], v[154:157], v[198:201], v[106:109]
	s_nop 0
	v_mfma_i32_16x16x64_i8 v[106:109], v[158:161], v[202:205], v[106:109]
	v_mfma_i32_16x16x64_i8 v[102:105], v[146:149], v[206:209], v[102:105]
	s_nop 0
	v_mfma_i32_16x16x64_i8 v[102:105], v[150:153], v[210:213], v[102:105]
	v_mfma_i32_16x16x64_i8 v[90:93], v[154:157], v[206:209], v[90:93]
	s_nop 0
	v_mfma_i32_16x16x64_i8 v[90:93], v[158:161], v[210:213], v[90:93]
	v_mfma_i32_16x16x64_i8 v[82:85], v[146:149], v[214:217], v[82:85]
	s_nop 0
	v_mfma_i32_16x16x64_i8 v[82:85], v[150:153], v[218:221], v[82:85]
	v_mfma_i32_16x16x64_i8 v[74:77], v[154:157], v[214:217], v[74:77]
	s_nop 0
	v_mfma_i32_16x16x64_i8 v[74:77], v[158:161], v[218:221], v[74:77]
	v_mfma_i32_16x16x64_i8 v[70:73], v[146:149], v[222:225], v[70:73]
	s_nop 0
	v_mfma_i32_16x16x64_i8 v[70:73], v[150:153], v[226:229], v[70:73]
	v_mfma_i32_16x16x64_i8 v[66:69], v[154:157], v[222:225], v[66:69]
	s_nop 0
	v_mfma_i32_16x16x64_i8 v[66:69], v[158:161], v[226:229], v[66:69]
	s_setprio 0
	s_barrier
	s_add_i32 s28, s52, s33
	v_lshl_add_u64 v[182:183], v[182:183], 0, s[10:11]
	s_mov_b32 m0, s28
	ds_read_b128 v[198:201], v194 offset:49152
	ds_read_b128 v[202:205], v194 offset:50176
	ds_read_b128 v[206:209], v194 offset:51200
	ds_read_b128 v[210:213], v194 offset:52224
	ds_read_b128 v[214:217], v194 offset:53248
	ds_read_b128 v[218:221], v194 offset:54272
	ds_read_b128 v[222:225], v194 offset:55296
	ds_read_b128 v[226:229], v194 offset:56320
	global_load_lds_dwordx4 v[182:183], off
	s_add_i32 m0, s28, 0x2000
	s_add_u32 s26, s26, 0x40080
	v_lshl_add_u64 v[182:183], v[184:185], 0, s[10:11]
	s_addc_u32 s27, s27, 0
	s_add_i32 s28, s53, s33
	global_load_lds_dwordx4 v[182:183], off
	v_lshl_add_u64 v[182:183], s[26:27], 0, v[166:167]
	s_mov_b32 m0, s28
	s_nop 0
	global_load_lds_dwordx4 v[182:183], off
	v_lshl_add_u64 v[182:183], s[26:27], 0, v[162:163]
	s_add_i32 m0, s28, 0x2000
	s_nop 0
	global_load_lds_dwordx4 v[182:183], off
	v_lshl_add_u64 v[182:183], v[186:187], 0, s[10:11]
	s_mov_b32 m0, s40
	s_nop 0
	global_load_lds_dwordx4 v[182:183], off
	v_lshl_add_u64 v[182:183], v[188:189], 0, s[10:11]
	s_mov_b32 m0, s41
	s_nop 0
	global_load_lds_dwordx4 v[182:183], off
	s_waitcnt vmcnt(8)
	s_waitcnt lgkmcnt(0)
	s_barrier
	s_setprio 1
	s_waitcnt lgkmcnt(0)
	v_mfma_i32_16x16x64_i8 v[62:65], v[130:133], v[198:201], v[62:65]
	s_nop 0
	v_mfma_i32_16x16x64_i8 v[62:65], v[134:137], v[202:205], v[62:65]
	v_mfma_i32_16x16x64_i8 v[58:61], v[138:141], v[198:201], v[58:61]
	s_nop 0
	v_mfma_i32_16x16x64_i8 v[58:61], v[142:145], v[202:205], v[58:61]
	v_mfma_i32_16x16x64_i8 v[54:57], v[130:133], v[206:209], v[54:57]
	s_nop 0
	v_mfma_i32_16x16x64_i8 v[54:57], v[134:137], v[210:213], v[54:57]
	v_mfma_i32_16x16x64_i8 v[46:49], v[138:141], v[206:209], v[46:49]
	s_nop 0
	v_mfma_i32_16x16x64_i8 v[46:49], v[142:145], v[210:213], v[46:49]
	v_mfma_i32_16x16x64_i8 v[38:41], v[130:133], v[214:217], v[38:41]
	s_nop 0
	v_mfma_i32_16x16x64_i8 v[38:41], v[134:137], v[218:221], v[38:41]
	v_mfma_i32_16x16x64_i8 v[30:33], v[138:141], v[214:217], v[30:33]
	s_nop 0
	v_mfma_i32_16x16x64_i8 v[30:33], v[142:145], v[218:221], v[30:33]
	v_mfma_i32_16x16x64_i8 v[22:25], v[130:133], v[222:225], v[22:25]
	s_nop 0
	v_mfma_i32_16x16x64_i8 v[22:25], v[134:137], v[226:229], v[22:25]
	v_mfma_i32_16x16x64_i8 v[14:17], v[138:141], v[222:225], v[14:17]
	s_nop 0
	v_mfma_i32_16x16x64_i8 v[14:17], v[142:145], v[226:229], v[14:17]
	s_setprio 0
	s_setprio 1
	v_mfma_i32_16x16x64_i8 v[50:53], v[146:149], v[198:201], v[50:53]
	s_nop 0
	v_mfma_i32_16x16x64_i8 v[50:53], v[150:153], v[202:205], v[50:53]
	v_mfma_i32_16x16x64_i8 v[42:45], v[154:157], v[198:201], v[42:45]
	s_nop 0
	v_mfma_i32_16x16x64_i8 v[42:45], v[158:161], v[202:205], v[42:45]
	v_mfma_i32_16x16x64_i8 v[34:37], v[146:149], v[206:209], v[34:37]
	s_nop 0
	v_mfma_i32_16x16x64_i8 v[34:37], v[150:153], v[210:213], v[34:37]
	v_mfma_i32_16x16x64_i8 v[26:29], v[154:157], v[206:209], v[26:29]
	s_nop 0
	v_mfma_i32_16x16x64_i8 v[26:29], v[158:161], v[210:213], v[26:29]
	v_mfma_i32_16x16x64_i8 v[18:21], v[146:149], v[214:217], v[18:21]
	s_nop 0
	v_mfma_i32_16x16x64_i8 v[18:21], v[150:153], v[218:221], v[18:21]
	v_mfma_i32_16x16x64_i8 v[10:13], v[154:157], v[214:217], v[10:13]
	s_nop 0
	v_mfma_i32_16x16x64_i8 v[10:13], v[158:161], v[218:221], v[10:13]
	v_mfma_i32_16x16x64_i8 v[6:9], v[146:149], v[222:225], v[6:9]
	s_nop 0
	v_mfma_i32_16x16x64_i8 v[6:9], v[150:153], v[226:229], v[6:9]
	v_mfma_i32_16x16x64_i8 v[2:5], v[154:157], v[222:225], v[2:5]
	s_nop 0
	v_mfma_i32_16x16x64_i8 v[2:5], v[158:161], v[226:229], v[2:5]
	s_setprio 0
	s_barrier
	s_add_i32 s51, s51, 2
	s_add_u32 s24, s24, 0x100
	s_addc_u32 s25, s25, 0
	s_add_u32 s49, s49, 0x100
	s_addc_u32 s50, s50, 0
	s_cmp_gt_u32 s51, 13
	s_cbranch_scc1 .Lpeel_exit_244

.Lq_skip:
.LBB0_754:
	s_mov_b32 s100, 0
	v_readlane_b32 s2, v250, 40
	v_readlane_b32 s3, v250, 41
	s_cmp_lt_i32 s2, 8
	s_cselect_b64 s[2:3], -1, 0
	s_and_b64 s[0:1], s[2:3], s[0:1]
	s_andn2_b64 vcc, exec, s[0:1]
	s_cbranch_vccnz .LBB0_805
	s_cmp_eq_u32 s97, 0x100
	s_cselect_b32 s98, 202, s97
	v_readfirstlane_b32 s30, v0
	s_lshr_b32 s30, s30, 6
	s_cmp_eq_u32 s97, 0x100
	s_cbranch_scc0 .Lq7_all
	s_cmpk_lt_i32 s74, 202
	s_cbranch_scc1 .Lq7_gemm
	s_sub_u32 s12, s74, 202
	s_lshl_b32 s12, s12, 3
	s_add_u32 s12, s12, s30
	s_add_u32 s12, s12, 0x5328
	s_movk_i32 s13, 432
	s_mov_b32 s14, 0x97e8
	s_mov_b32 s46, 7
	s_branch .Lq_conv

.LBB0_763:
	s_ashr_i32 s17, s16, 31
	s_lshl_b64 s[18:19], s[16:17], 19
	s_add_u32 s18, s72, s18
	s_addc_u32 s19, s73, s19
	s_and_b64 s[20:21], s[0:1], exec
	s_cselect_b32 s17, s19, s25
	s_cselect_b32 s47, s18, s24
	s_ashr_i32 s15, s14, 31
	s_lshl_b64 s[20:21], s[14:15], 19
	s_add_u32 s20, s30, s20
	s_addc_u32 s21, s31, s21
	s_and_b64 s[28:29], s[0:1], exec
	s_cselect_b32 s15, s21, s27
	s_cselect_b32 s48, s20, s26
	s_add_u32 s24, s24, 0x40080
	s_addc_u32 s25, s25, 0
	s_add_u32 s49, s26, 0x100
	v_mov_b32_e32 v2, 0
	s_addc_u32 s50, s27, 0
	s_mov_b32 s51, -2
	v_mov_b32_e32 v3, v2
	v_mov_b32_e32 v4, v2
	v_mov_b32_e32 v5, v2
	v_mov_b32_e32 v6, v2
	v_mov_b32_e32 v7, v2
	v_mov_b32_e32 v8, v2
	v_mov_b32_e32 v9, v2
	v_mov_b32_e32 v14, v2
	v_mov_b32_e32 v15, v2
	v_mov_b32_e32 v16, v2
	v_mov_b32_e32 v17, v2
	s_waitcnt vmcnt(0)
	ds_read_b128 v[158:161], v193
	ds_read_b128 v[154:157], v193 offset:1024
	ds_read_b128 v[150:153], v193 offset:2048
	ds_read_b128 v[146:149], v193 offset:3072
	ds_read_b128 v[142:145], v194
	ds_read_b128 v[138:141], v194 offset:1024
	ds_read_b128 v[134:137], v194 offset:2048
	ds_read_b128 v[130:133], v194 offset:3072
	s_add_u32 s26, s24, 0xfffc0080
	s_addc_u32 s27, s25, -1
	s_cmp_eq_u32 s51, 12
	s_cselect_b32 s29, s17, s27
	s_cselect_b32 s28, s47, s26
	s_cselect_b32 s27, s15, s50
	s_cselect_b32 s26, s48, s49
	v_lshl_add_u64 v[224:225], s[24:25], 0, v[170:171]
	s_add_i32 m0, s23, 0xc000
	ds_read_b128 v[184:187], v196
	ds_read_b128 v[188:191], v196 offset:1024
	ds_read_b128 v[200:203], v196 offset:2048
	ds_read_b128 v[204:207], v196 offset:3072
	ds_read_b128 v[208:211], v196 offset:4096
	ds_read_b128 v[212:215], v196 offset:5120
	ds_read_b128 v[216:219], v196 offset:6144
	ds_read_b128 v[220:223], v196 offset:7168
	global_load_lds_dwordx4 v[224:225], off
	v_lshl_add_u64 v[224:225], s[24:25], 0, v[172:173]
	s_add_i32 m0, s23, 0xe000
	s_nop 0
	global_load_lds_dwordx4 v[224:225], off
	s_cmp_lg_u32 s100, 0
	s_cbranch_scc1 .Lpw_764_0
	s_waitcnt vmcnt(8)
.Lpw_764_0:
	s_waitcnt lgkmcnt(0)
	s_barrier
	s_setprio 1
	s_waitcnt lgkmcnt(0)
	v_mfma_i32_16x16x64_i8 v[126:129], v[158:161], v[184:187], 0
	s_nop 0
	v_mfma_i32_16x16x64_i8 v[126:129], v[154:157], v[188:191], v[126:129]
	v_mfma_i32_16x16x64_i8 v[118:121], v[150:153], v[184:187], 0
	s_nop 0
	v_mfma_i32_16x16x64_i8 v[118:121], v[146:149], v[188:191], v[118:121]
	v_mfma_i32_16x16x64_i8 v[114:117], v[158:161], v[200:203], 0
	s_nop 0
	v_mfma_i32_16x16x64_i8 v[114:117], v[154:157], v[204:207], v[114:117]
	v_mfma_i32_16x16x64_i8 v[110:113], v[150:153], v[200:203], 0
	s_nop 0
	v_mfma_i32_16x16x64_i8 v[110:113], v[146:149], v[204:207], v[110:113]
	v_mfma_i32_16x16x64_i8 v[94:97], v[158:161], v[208:211], 0
	s_nop 0
	v_mfma_i32_16x16x64_i8 v[94:97], v[154:157], v[212:215], v[94:97]
	v_mfma_i32_16x16x64_i8 v[86:89], v[150:153], v[208:211], 0
	s_nop 0
	v_mfma_i32_16x16x64_i8 v[86:89], v[146:149], v[212:215], v[86:89]
	v_mfma_i32_16x16x64_i8 v[82:85], v[158:161], v[216:219], 0
	s_nop 0
	v_mfma_i32_16x16x64_i8 v[82:85], v[154:157], v[220:223], v[82:85]
	v_mfma_i32_16x16x64_i8 v[74:77], v[150:153], v[216:219], 0
	s_nop 0
	v_mfma_i32_16x16x64_i8 v[74:77], v[146:149], v[220:223], v[74:77]
	s_setprio 0
	s_setprio 1
	v_mfma_i32_16x16x64_i8 v[122:125], v[142:145], v[184:187], 0
	s_nop 0
	v_mfma_i32_16x16x64_i8 v[122:125], v[138:141], v[188:191], v[122:125]
	v_mfma_i32_16x16x64_i8 v[106:109], v[134:137], v[184:187], 0
	s_nop 0
	v_mfma_i32_16x16x64_i8 v[106:109], v[130:133], v[188:191], v[106:109]
	v_mfma_i32_16x16x64_i8 v[102:105], v[142:145], v[200:203], 0
	s_nop 0
	v_mfma_i32_16x16x64_i8 v[102:105], v[138:141], v[204:207], v[102:105]
	v_mfma_i32_16x16x64_i8 v[98:101], v[134:137], v[200:203], 0
	s_nop 0
	v_mfma_i32_16x16x64_i8 v[98:101], v[130:133], v[204:207], v[98:101]
	v_mfma_i32_16x16x64_i8 v[90:93], v[142:145], v[208:211], 0
	s_nop 0
	v_mfma_i32_16x16x64_i8 v[90:93], v[138:141], v[212:215], v[90:93]
	v_mfma_i32_16x16x64_i8 v[78:81], v[134:137], v[208:211], 0
	s_nop 0
	v_mfma_i32_16x16x64_i8 v[78:81], v[130:133], v[212:215], v[78:81]
	v_mfma_i32_16x16x64_i8 v[70:73], v[142:145], v[216:219], 0
	s_nop 0
	v_mfma_i32_16x16x64_i8 v[70:73], v[138:141], v[220:223], v[70:73]
	v_mfma_i32_16x16x64_i8 v[66:69], v[134:137], v[216:219], 0
	s_nop 0
	v_mfma_i32_16x16x64_i8 v[66:69], v[130:133], v[220:223], v[66:69]
	s_setprio 0
	s_barrier
	s_add_i32 s52, s43, s33
	v_lshl_add_u64 v[184:185], s[26:27], 0, v[166:167]
	s_mov_b32 m0, s52
	ds_read_b128 v[200:203], v196 offset:16384
	ds_read_b128 v[204:207], v196 offset:17408
	ds_read_b128 v[208:211], v196 offset:18432
	ds_read_b128 v[212:215], v196 offset:19456
	ds_read_b128 v[216:219], v196 offset:20480
	ds_read_b128 v[220:223], v196 offset:21504
	ds_read_b128 v[224:227], v196 offset:22528
	ds_read_b128 v[228:231], v196 offset:23552
	global_load_lds_dwordx4 v[184:185], off
	s_add_i32 m0, s52, 0x2000
	s_add_u32 s52, s26, 0x40000
	v_lshl_add_u64 v[186:187], s[26:27], 0, v[162:163]
	s_addc_u32 s53, s27, 0
	s_add_i32 s54, s44, s33
	global_load_lds_dwordx4 v[186:187], off
	v_lshl_add_u64 v[188:189], s[52:53], 0, v[166:167]
	s_mov_b32 m0, s54
	v_lshl_add_u64 v[190:191], s[28:29], 0, v[164:165]
	global_load_lds_dwordx4 v[188:189], off
	v_lshl_add_u64 v[188:189], s[52:53], 0, v[162:163]
	s_add_i32 m0, s54, 0x2000
	s_nop 0
	global_load_lds_dwordx4 v[188:189], off
	v_lshl_add_u64 v[188:189], s[28:29], 0, v[168:169]
	s_mov_b32 m0, s23
	s_nop 0
	global_load_lds_dwordx4 v[188:189], off
	s_mov_b32 m0, s36
	s_nop 0
	global_load_lds_dwordx4 v[190:191], off
	s_cmp_lg_u32 s100, 0
	s_cbranch_scc1 .Lpw_764_1
	s_waitcnt vmcnt(8)
.Lpw_764_1:
	s_add_u32 s100, s100, 1
	s_waitcnt lgkmcnt(0)
	s_barrier
	s_setprio 1
	s_waitcnt lgkmcnt(0)
	v_mfma_i32_16x16x64_i8 v[62:65], v[158:161], v[200:203], 0
	s_nop 0
	v_mfma_i32_16x16x64_i8 v[62:65], v[154:157], v[204:207], v[62:65]
	v_mfma_i32_16x16x64_i8 v[58:61], v[150:153], v[200:203], 0
	s_nop 0
	v_mfma_i32_16x16x64_i8 v[58:61], v[146:149], v[204:207], v[58:61]
	v_mfma_i32_16x16x64_i8 v[50:53], v[158:161], v[208:211], 0
	s_nop 0
	v_mfma_i32_16x16x64_i8 v[50:53], v[154:157], v[212:215], v[50:53]
	v_mfma_i32_16x16x64_i8 v[42:45], v[150:153], v[208:211], 0
	s_nop 0
	v_mfma_i32_16x16x64_i8 v[42:45], v[146:149], v[212:215], v[42:45]
	v_mfma_i32_16x16x64_i8 v[34:37], v[158:161], v[216:219], 0
	s_nop 0
	v_mfma_i32_16x16x64_i8 v[34:37], v[154:157], v[220:223], v[34:37]
	v_mfma_i32_16x16x64_i8 v[26:29], v[150:153], v[216:219], 0
	s_nop 0
	v_mfma_i32_16x16x64_i8 v[26:29], v[146:149], v[220:223], v[26:29]
	v_mfma_i32_16x16x64_i8 v[18:21], v[158:161], v[224:227], 0
	s_nop 0
	v_mfma_i32_16x16x64_i8 v[18:21], v[154:157], v[228:231], v[18:21]
	v_mfma_i32_16x16x64_i8 v[10:13], v[150:153], v[224:227], 0
	s_nop 0
	v_mfma_i32_16x16x64_i8 v[10:13], v[146:149], v[228:231], v[10:13]
	s_setprio 0
	s_setprio 1
	v_mfma_i32_16x16x64_i8 v[54:57], v[142:145], v[200:203], 0
	s_nop 0
	v_mfma_i32_16x16x64_i8 v[54:57], v[138:141], v[204:207], v[54:57]
	v_mfma_i32_16x16x64_i8 v[46:49], v[134:137], v[200:203], 0
	s_nop 0
	v_mfma_i32_16x16x64_i8 v[46:49], v[130:133], v[204:207], v[46:49]
	v_mfma_i32_16x16x64_i8 v[38:41], v[142:145], v[208:211], 0
	s_nop 0
	v_mfma_i32_16x16x64_i8 v[38:41], v[138:141], v[212:215], v[38:41]
	v_mfma_i32_16x16x64_i8 v[30:33], v[134:137], v[208:211], 0
	s_nop 0
	v_mfma_i32_16x16x64_i8 v[30:33], v[130:133], v[212:215], v[30:33]
	v_mfma_i32_16x16x64_i8 v[22:25], v[142:145], v[216:219], 0
	s_nop 0
	v_mfma_i32_16x16x64_i8 v[22:25], v[138:141], v[220:223], v[22:25]
	v_mfma_i32_16x16x64_i8 v[14:17], v[134:137], v[216:219], 0
	s_nop 0
	v_mfma_i32_16x16x64_i8 v[14:17], v[130:133], v[220:223], v[14:17]
	v_mfma_i32_16x16x64_i8 v[6:9], v[142:145], v[224:227], 0
	s_nop 0
	v_mfma_i32_16x16x64_i8 v[6:9], v[138:141], v[228:231], v[6:9]
	v_mfma_i32_16x16x64_i8 v[2:5], v[134:137], v[224:227], 0
	s_nop 0
	v_mfma_i32_16x16x64_i8 v[2:5], v[130:133], v[228:231], v[2:5]
	s_setprio 0
	s_barrier
	s_add_i32 s52, 0, 0x18000
	s_add_i32 s53, 0, 0x1c000
	v_add_u32_e32 v142, s52, v183
	v_add_u32_e32 v158, s53, v183
	ds_read_b128 v[130:133], v142
	ds_read_b128 v[134:137], v142 offset:1024
	ds_read_b128 v[138:141], v142 offset:2048
	ds_read_b128 v[142:145], v142 offset:3072
	ds_read_b128 v[146:149], v158
	ds_read_b128 v[150:153], v158 offset:1024
	ds_read_b128 v[154:157], v158 offset:2048
	ds_read_b128 v[158:161], v158 offset:3072
	s_add_u32 s28, s28, 0x40000
	s_addc_u32 s29, s29, 0
	s_mov_b32 m0, s37
	v_lshl_add_u64 v[232:233], s[28:29], 0, v[168:169]
	ds_read_b128 v[200:203], v196 offset:32768
	ds_read_b128 v[204:207], v196 offset:33792
	ds_read_b128 v[208:211], v196 offset:34816
	ds_read_b128 v[212:215], v196 offset:35840
	ds_read_b128 v[216:219], v196 offset:36864
	ds_read_b128 v[220:223], v196 offset:37888
	ds_read_b128 v[224:227], v196 offset:38912
	ds_read_b128 v[228:231], v196 offset:39936
	global_load_lds_dwordx4 v[232:233], off
	v_lshl_add_u64 v[232:233], s[28:29], 0, v[164:165]
	s_mov_b32 m0, s38
	s_nop 0
	global_load_lds_dwordx4 v[232:233], off
	s_waitcnt vmcnt(8)
	s_waitcnt lgkmcnt(0)
	s_barrier
	s_setprio 1
	s_waitcnt lgkmcnt(0)
	v_mfma_i32_16x16x64_i8 v[126:129], v[130:133], v[200:203], v[126:129]
	s_nop 0
	v_mfma_i32_16x16x64_i8 v[126:129], v[134:137], v[204:207], v[126:129]
	v_mfma_i32_16x16x64_i8 v[118:121], v[138:141], v[200:203], v[118:121]
	s_nop 0
	v_mfma_i32_16x16x64_i8 v[118:121], v[142:145], v[204:207], v[118:121]
	v_mfma_i32_16x16x64_i8 v[114:117], v[130:133], v[208:211], v[114:117]
	s_nop 0
	v_mfma_i32_16x16x64_i8 v[114:117], v[134:137], v[212:215], v[114:117]
	v_mfma_i32_16x16x64_i8 v[110:113], v[138:141], v[208:211], v[110:113]
	s_nop 0
	v_mfma_i32_16x16x64_i8 v[110:113], v[142:145], v[212:215], v[110:113]
	v_mfma_i32_16x16x64_i8 v[94:97], v[130:133], v[216:219], v[94:97]
	s_nop 0
	v_mfma_i32_16x16x64_i8 v[94:97], v[134:137], v[220:223], v[94:97]
	v_mfma_i32_16x16x64_i8 v[86:89], v[138:141], v[216:219], v[86:89]
	s_nop 0
	v_mfma_i32_16x16x64_i8 v[86:89], v[142:145], v[220:223], v[86:89]
	v_mfma_i32_16x16x64_i8 v[82:85], v[130:133], v[224:227], v[82:85]
	s_nop 0
	v_mfma_i32_16x16x64_i8 v[82:85], v[134:137], v[228:231], v[82:85]
	v_mfma_i32_16x16x64_i8 v[74:77], v[138:141], v[224:227], v[74:77]
	s_nop 0
	v_mfma_i32_16x16x64_i8 v[74:77], v[142:145], v[228:231], v[74:77]
	s_setprio 0
	s_setprio 1
	v_mfma_i32_16x16x64_i8 v[122:125], v[146:149], v[200:203], v[122:125]
	s_nop 0
	v_mfma_i32_16x16x64_i8 v[122:125], v[150:153], v[204:207], v[122:125]
	v_mfma_i32_16x16x64_i8 v[106:109], v[154:157], v[200:203], v[106:109]
	s_nop 0
	v_mfma_i32_16x16x64_i8 v[106:109], v[158:161], v[204:207], v[106:109]
	v_mfma_i32_16x16x64_i8 v[102:105], v[146:149], v[208:211], v[102:105]
	s_nop 0
	v_mfma_i32_16x16x64_i8 v[102:105], v[150:153], v[212:215], v[102:105]
	v_mfma_i32_16x16x64_i8 v[98:101], v[154:157], v[208:211], v[98:101]
	s_nop 0
	v_mfma_i32_16x16x64_i8 v[98:101], v[158:161], v[212:215], v[98:101]
	v_mfma_i32_16x16x64_i8 v[90:93], v[146:149], v[216:219], v[90:93]
	s_nop 0
	v_mfma_i32_16x16x64_i8 v[90:93], v[150:153], v[220:223], v[90:93]
	v_mfma_i32_16x16x64_i8 v[78:81], v[154:157], v[216:219], v[78:81]
	s_nop 0
	v_mfma_i32_16x16x64_i8 v[78:81], v[158:161], v[220:223], v[78:81]
	v_mfma_i32_16x16x64_i8 v[70:73], v[146:149], v[224:227], v[70:73]
	s_nop 0
	v_mfma_i32_16x16x64_i8 v[70:73], v[150:153], v[228:231], v[70:73]
	v_mfma_i32_16x16x64_i8 v[66:69], v[154:157], v[224:227], v[66:69]
	s_nop 0
	v_mfma_i32_16x16x64_i8 v[66:69], v[158:161], v[228:231], v[66:69]
	s_setprio 0
	s_barrier
	s_add_i32 s28, s52, s33
	v_lshl_add_u64 v[184:185], v[184:185], 0, s[10:11]
	s_mov_b32 m0, s28
	ds_read_b128 v[200:203], v196 offset:49152
	ds_read_b128 v[204:207], v196 offset:50176
	ds_read_b128 v[208:211], v196 offset:51200
	ds_read_b128 v[212:215], v196 offset:52224
	ds_read_b128 v[216:219], v196 offset:53248
	ds_read_b128 v[220:223], v196 offset:54272
	ds_read_b128 v[224:227], v196 offset:55296
	ds_read_b128 v[228:231], v196 offset:56320
	global_load_lds_dwordx4 v[184:185], off
	s_add_i32 m0, s28, 0x2000
	s_add_u32 s26, s26, 0x40080
	v_lshl_add_u64 v[184:185], v[186:187], 0, s[10:11]
	s_addc_u32 s27, s27, 0
	s_add_i32 s28, s53, s33
	global_load_lds_dwordx4 v[184:185], off
	v_lshl_add_u64 v[184:185], s[26:27], 0, v[166:167]
	s_mov_b32 m0, s28
	s_nop 0
	global_load_lds_dwordx4 v[184:185], off
	v_lshl_add_u64 v[184:185], s[26:27], 0, v[162:163]
	s_add_i32 m0, s28, 0x2000
	s_nop 0
	global_load_lds_dwordx4 v[184:185], off
	v_lshl_add_u64 v[184:185], v[188:189], 0, s[10:11]
	s_mov_b32 m0, s40
	s_nop 0
	global_load_lds_dwordx4 v[184:185], off
	v_lshl_add_u64 v[184:185], v[190:191], 0, s[10:11]
	s_mov_b32 m0, s41
	s_nop 0
	global_load_lds_dwordx4 v[184:185], off
	s_waitcnt vmcnt(8)
	s_waitcnt lgkmcnt(0)
	s_barrier
	s_setprio 1
	s_waitcnt lgkmcnt(0)
	v_mfma_i32_16x16x64_i8 v[62:65], v[130:133], v[200:203], v[62:65]
	s_nop 0
	v_mfma_i32_16x16x64_i8 v[62:65], v[134:137], v[204:207], v[62:65]
	v_mfma_i32_16x16x64_i8 v[58:61], v[138:141], v[200:203], v[58:61]
	s_nop 0
	v_mfma_i32_16x16x64_i8 v[58:61], v[142:145], v[204:207], v[58:61]
	v_mfma_i32_16x16x64_i8 v[50:53], v[130:133], v[208:211], v[50:53]
	s_nop 0
	v_mfma_i32_16x16x64_i8 v[50:53], v[134:137], v[212:215], v[50:53]
	v_mfma_i32_16x16x64_i8 v[42:45], v[138:141], v[208:211], v[42:45]
	s_nop 0
	v_mfma_i32_16x16x64_i8 v[42:45], v[142:145], v[212:215], v[42:45]
	v_mfma_i32_16x16x64_i8 v[34:37], v[130:133], v[216:219], v[34:37]
	s_nop 0
	v_mfma_i32_16x16x64_i8 v[34:37], v[134:137], v[220:223], v[34:37]
	v_mfma_i32_16x16x64_i8 v[26:29], v[138:141], v[216:219], v[26:29]
	s_nop 0
	v_mfma_i32_16x16x64_i8 v[26:29], v[142:145], v[220:223], v[26:29]
	v_mfma_i32_16x16x64_i8 v[18:21], v[130:133], v[224:227], v[18:21]
	s_nop 0
	v_mfma_i32_16x16x64_i8 v[18:21], v[134:137], v[228:231], v[18:21]
	v_mfma_i32_16x16x64_i8 v[10:13], v[138:141], v[224:227], v[10:13]
	s_nop 0
	v_mfma_i32_16x16x64_i8 v[10:13], v[142:145], v[228:231], v[10:13]
	s_setprio 0
	s_setprio 1
	v_mfma_i32_16x16x64_i8 v[54:57], v[146:149], v[200:203], v[54:57]
	s_nop 0
	v_mfma_i32_16x16x64_i8 v[54:57], v[150:153], v[204:207], v[54:57]
	v_mfma_i32_16x16x64_i8 v[46:49], v[154:157], v[200:203], v[46:49]
	s_nop 0
	v_mfma_i32_16x16x64_i8 v[46:49], v[158:161], v[204:207], v[46:49]
	v_mfma_i32_16x16x64_i8 v[38:41], v[146:149], v[208:211], v[38:41]
	s_nop 0
	v_mfma_i32_16x16x64_i8 v[38:41], v[150:153], v[212:215], v[38:41]
	v_mfma_i32_16x16x64_i8 v[30:33], v[154:157], v[208:211], v[30:33]
	s_nop 0
	v_mfma_i32_16x16x64_i8 v[30:33], v[158:161], v[212:215], v[30:33]
	v_mfma_i32_16x16x64_i8 v[22:25], v[146:149], v[216:219], v[22:25]
	s_nop 0
	v_mfma_i32_16x16x64_i8 v[22:25], v[150:153], v[220:223], v[22:25]
	v_mfma_i32_16x16x64_i8 v[14:17], v[154:157], v[216:219], v[14:17]
	s_nop 0
	v_mfma_i32_16x16x64_i8 v[14:17], v[158:161], v[220:223], v[14:17]
	v_mfma_i32_16x16x64_i8 v[6:9], v[146:149], v[224:227], v[6:9]
	s_nop 0
	v_mfma_i32_16x16x64_i8 v[6:9], v[150:153], v[228:231], v[6:9]
	v_mfma_i32_16x16x64_i8 v[2:5], v[154:157], v[224:227], v[2:5]
	s_nop 0
	v_mfma_i32_16x16x64_i8 v[2:5], v[158:161], v[228:231], v[2:5]
	s_setprio 0
	s_barrier
	s_add_i32 s51, s51, 2
	s_add_u32 s24, s24, 0x100
	s_addc_u32 s25, s25, 0
	s_add_u32 s49, s49, 0x100
	s_addc_u32 s50, s50, 0
	s_cmp_gt_u32 s51, 13
	s_cbranch_scc1 .Lpeel_exit_764

.LBB0_1707:
	s_mov_b32 s100, 0
	v_readlane_b32 s4, v250, 40
	s_cmp_lt_i32 s4, 18
	v_readlane_b32 s5, v250, 41
	s_cselect_b64 s[0:1], -1, 0
	s_cmp_gt_i32 s4, 17
	s_cselect_b64 s[2:3], -1, 0
	s_cmp_lt_i32 s5, 18
	s_cselect_b64 s[4:5], -1, 0
	s_or_b64 s[2:3], s[2:3], s[4:5]
	s_and_b64 vcc, exec, s[2:3]
	s_cbranch_vccnz .LBB0_1731
	v_readfirstlane_b32 s8, v0
	s_lshr_b32 s8, s8, 6
	s_cmp_eq_u32 s97, 0x100
	s_cbranch_scc0 .Lcv17_all
	s_cmpk_lt_i32 s74, 0xe0
	s_cbranch_scc1 .Lcv17_gemm
	s_sub_u32 s6, s74, 0xe0
	s_lshl_b32 s6, s6, 3
	s_add_u32 s6, s6, s8
	s_movk_i32 s7, 0x100
	s_mov_b32 s17, 0
	s_branch .Lcv17_conv

.LBB0_1722:
	s_ashr_i32 s37, s36, 31
	s_lshl_b64 s[40:41], s[36:37], 19
	s_add_u32 s40, s63, s40
	s_addc_u32 s41, s64, s41
	s_and_b64 s[44:45], s[42:43], exec
	s_cselect_b32 s37, s41, s51
	s_cselect_b32 s84, s40, s50
	s_ashr_i32 s39, s38, 31
	s_lshl_b64 s[44:45], s[38:39], 19
	s_add_u32 s44, s65, s44
	s_addc_u32 s45, s66, s45
	s_and_b64 s[54:55], s[42:43], exec
	s_cselect_b32 s39, s45, s53
	s_cselect_b32 s85, s44, s52
	s_add_u32 s50, s50, 0x40080
	s_addc_u32 s51, s51, 0
	s_add_u32 s86, s52, 0x100
	v_mov_b32_e32 v2, 0
	s_addc_u32 s87, s53, 0
	s_mov_b32 s88, -2
	ds_read_b128 v[158:161], v187
	ds_read_b128 v[154:157], v187 offset:1024
	ds_read_b128 v[150:153], v187 offset:2048
	ds_read_b128 v[146:149], v187 offset:3072
	ds_read_b128 v[142:145], v188
	ds_read_b128 v[138:141], v188 offset:1024
	ds_read_b128 v[134:137], v188 offset:2048
	ds_read_b128 v[130:133], v188 offset:3072
	s_add_u32 s52, s50, 0xfffc0080
	s_addc_u32 s53, s51, -1
	s_cmp_eq_u32 s88, 12
	s_cselect_b32 s55, s37, s53
	s_cselect_b32 s54, s84, s52
	s_cselect_b32 s53, s39, s87
	s_cselect_b32 s52, s85, s86
	v_lshl_add_u64 v[214:215], s[50:51], 0, v[170:171]
	s_add_i32 m0, s47, 0xc000
	ds_read_b128 v[174:177], v189
	ds_read_b128 v[182:185], v189 offset:1024
	ds_read_b128 v[190:193], v189 offset:2048
	ds_read_b128 v[194:197], v189 offset:3072
	ds_read_b128 v[198:201], v189 offset:4096
	ds_read_b128 v[202:205], v189 offset:5120
	ds_read_b128 v[206:209], v189 offset:6144
	ds_read_b128 v[210:213], v189 offset:7168
	global_load_lds_dwordx4 v[214:215], off
	v_lshl_add_u64 v[214:215], s[50:51], 0, v[172:173]
	s_add_i32 m0, s47, 0xe000
	s_nop 0
	global_load_lds_dwordx4 v[214:215], off
	s_cmp_lg_u32 s100, 0
	s_cbranch_scc1 .Lpw_1723_0
	s_waitcnt vmcnt(8)
.Lpw_1723_0:
	s_waitcnt lgkmcnt(0)
	s_barrier
	s_setprio 1
	s_waitcnt lgkmcnt(0)
	v_mfma_i32_16x16x64_i8 v[126:129], v[158:161], v[174:177], 0
	s_nop 0
	v_mfma_i32_16x16x64_i8 v[126:129], v[154:157], v[182:185], v[126:129]
	v_mfma_i32_16x16x64_i8 v[118:121], v[150:153], v[174:177], 0
	s_nop 0
	v_mfma_i32_16x16x64_i8 v[118:121], v[146:149], v[182:185], v[118:121]
	v_mfma_i32_16x16x64_i8 v[114:117], v[158:161], v[190:193], 0
	s_nop 0
	v_mfma_i32_16x16x64_i8 v[114:117], v[154:157], v[194:197], v[114:117]
	v_mfma_i32_16x16x64_i8 v[110:113], v[150:153], v[190:193], 0
	s_nop 0
	v_mfma_i32_16x16x64_i8 v[110:113], v[146:149], v[194:197], v[110:113]
	v_mfma_i32_16x16x64_i8 v[94:97], v[158:161], v[198:201], 0
	s_nop 0
	v_mfma_i32_16x16x64_i8 v[94:97], v[154:157], v[202:205], v[94:97]
	v_mfma_i32_16x16x64_i8 v[86:89], v[150:153], v[198:201], 0
	s_nop 0
	v_mfma_i32_16x16x64_i8 v[86:89], v[146:149], v[202:205], v[86:89]
	v_mfma_i32_16x16x64_i8 v[82:85], v[158:161], v[206:209], 0
	s_nop 0
	v_mfma_i32_16x16x64_i8 v[82:85], v[154:157], v[210:213], v[82:85]
	v_mfma_i32_16x16x64_i8 v[74:77], v[150:153], v[206:209], 0
	s_nop 0
	v_mfma_i32_16x16x64_i8 v[74:77], v[146:149], v[210:213], v[74:77]
	s_setprio 0
	s_setprio 1
	v_mfma_i32_16x16x64_i8 v[122:125], v[142:145], v[174:177], 0
	s_nop 0
	v_mfma_i32_16x16x64_i8 v[122:125], v[138:141], v[182:185], v[122:125]
	v_mfma_i32_16x16x64_i8 v[106:109], v[134:137], v[174:177], 0
	s_nop 0
	v_mfma_i32_16x16x64_i8 v[106:109], v[130:133], v[182:185], v[106:109]
	v_mfma_i32_16x16x64_i8 v[102:105], v[142:145], v[190:193], 0
	s_nop 0
	v_mfma_i32_16x16x64_i8 v[102:105], v[138:141], v[194:197], v[102:105]
	v_mfma_i32_16x16x64_i8 v[98:101], v[134:137], v[190:193], 0
	s_nop 0
	v_mfma_i32_16x16x64_i8 v[98:101], v[130:133], v[194:197], v[98:101]
	v_mfma_i32_16x16x64_i8 v[90:93], v[142:145], v[198:201], 0
	s_nop 0
	v_mfma_i32_16x16x64_i8 v[90:93], v[138:141], v[202:205], v[90:93]
	v_mfma_i32_16x16x64_i8 v[78:81], v[134:137], v[198:201], 0
	s_nop 0
	v_mfma_i32_16x16x64_i8 v[78:81], v[130:133], v[202:205], v[78:81]
	v_mfma_i32_16x16x64_i8 v[70:73], v[142:145], v[206:209], 0
	s_nop 0
	v_mfma_i32_16x16x64_i8 v[70:73], v[138:141], v[210:213], v[70:73]
	v_mfma_i32_16x16x64_i8 v[66:69], v[134:137], v[206:209], 0
	s_nop 0
	v_mfma_i32_16x16x64_i8 v[66:69], v[130:133], v[210:213], v[66:69]
	s_setprio 0
	s_barrier
	s_add_i32 s89, s79, s67
	v_lshl_add_u64 v[174:175], s[52:53], 0, v[164:165]
	s_mov_b32 m0, s89
	ds_read_b128 v[190:193], v189 offset:16384
	ds_read_b128 v[194:197], v189 offset:17408
	ds_read_b128 v[198:201], v189 offset:18432
	ds_read_b128 v[202:205], v189 offset:19456
	ds_read_b128 v[206:209], v189 offset:20480
	ds_read_b128 v[210:213], v189 offset:21504
	ds_read_b128 v[214:217], v189 offset:22528
	ds_read_b128 v[218:221], v189 offset:23552
	global_load_lds_dwordx4 v[174:175], off
	s_add_i32 m0, s89, 0x2000
	s_add_u32 s90, s52, 0x40000
	v_lshl_add_u64 v[176:177], s[52:53], 0, v[168:169]
	s_addc_u32 s91, s53, 0
	s_add_i32 s89, s80, s67
	global_load_lds_dwordx4 v[176:177], off
	v_lshl_add_u64 v[182:183], s[90:91], 0, v[164:165]
	s_mov_b32 m0, s89
	v_lshl_add_u64 v[184:185], s[54:55], 0, v[166:167]
	global_load_lds_dwordx4 v[182:183], off
	v_lshl_add_u64 v[182:183], s[90:91], 0, v[168:169]
	s_add_i32 m0, s89, 0x2000
	s_nop 0
	global_load_lds_dwordx4 v[182:183], off
	v_lshl_add_u64 v[182:183], s[54:55], 0, v[162:163]
	s_mov_b32 m0, s47
	s_nop 0
	global_load_lds_dwordx4 v[182:183], off
	s_mov_b32 m0, s49
	s_nop 0
	global_load_lds_dwordx4 v[184:185], off
	s_cmp_lg_u32 s100, 0
	s_cbranch_scc1 .Lpw_1723_1
	s_waitcnt vmcnt(8)
.Lpw_1723_1:
	s_add_u32 s100, s100, 1
	s_waitcnt lgkmcnt(0)
	s_barrier
	s_setprio 1
	s_waitcnt lgkmcnt(0)
	v_mfma_i32_16x16x64_i8 v[62:65], v[158:161], v[190:193], 0
	s_nop 0
	v_mfma_i32_16x16x64_i8 v[62:65], v[154:157], v[194:197], v[62:65]
	v_mfma_i32_16x16x64_i8 v[58:61], v[150:153], v[190:193], 0
	s_nop 0
	v_mfma_i32_16x16x64_i8 v[58:61], v[146:149], v[194:197], v[58:61]
	v_mfma_i32_16x16x64_i8 v[50:53], v[158:161], v[198:201], 0
	s_nop 0
	v_mfma_i32_16x16x64_i8 v[50:53], v[154:157], v[202:205], v[50:53]
	v_mfma_i32_16x16x64_i8 v[42:45], v[150:153], v[198:201], 0
	s_nop 0
	v_mfma_i32_16x16x64_i8 v[42:45], v[146:149], v[202:205], v[42:45]
	v_mfma_i32_16x16x64_i8 v[34:37], v[158:161], v[206:209], 0
	s_nop 0
	v_mfma_i32_16x16x64_i8 v[34:37], v[154:157], v[210:213], v[34:37]
	v_mfma_i32_16x16x64_i8 v[26:29], v[150:153], v[206:209], 0
	s_nop 0
	v_mfma_i32_16x16x64_i8 v[26:29], v[146:149], v[210:213], v[26:29]
	v_mfma_i32_16x16x64_i8 v[18:21], v[158:161], v[214:217], 0
	s_nop 0
	v_mfma_i32_16x16x64_i8 v[18:21], v[154:157], v[218:221], v[18:21]
	v_mfma_i32_16x16x64_i8 v[10:13], v[150:153], v[214:217], 0
	s_nop 0
	v_mfma_i32_16x16x64_i8 v[10:13], v[146:149], v[218:221], v[10:13]
	s_setprio 0
	s_setprio 1
	v_mfma_i32_16x16x64_i8 v[54:57], v[142:145], v[190:193], 0
	s_nop 0
	v_mfma_i32_16x16x64_i8 v[54:57], v[138:141], v[194:197], v[54:57]
	v_mfma_i32_16x16x64_i8 v[46:49], v[134:137], v[190:193], 0
	s_nop 0
	v_mfma_i32_16x16x64_i8 v[46:49], v[130:133], v[194:197], v[46:49]
	v_mfma_i32_16x16x64_i8 v[38:41], v[142:145], v[198:201], 0
	s_nop 0
	v_mfma_i32_16x16x64_i8 v[38:41], v[138:141], v[202:205], v[38:41]
	v_mfma_i32_16x16x64_i8 v[30:33], v[134:137], v[198:201], 0
	s_nop 0
	v_mfma_i32_16x16x64_i8 v[30:33], v[130:133], v[202:205], v[30:33]
	v_mfma_i32_16x16x64_i8 v[22:25], v[142:145], v[206:209], 0
	s_nop 0
	v_mfma_i32_16x16x64_i8 v[22:25], v[138:141], v[210:213], v[22:25]
	v_mfma_i32_16x16x64_i8 v[14:17], v[134:137], v[206:209], 0
	s_nop 0
	v_mfma_i32_16x16x64_i8 v[14:17], v[130:133], v[210:213], v[14:17]
	v_mfma_i32_16x16x64_i8 v[6:9], v[142:145], v[214:217], 0
	s_nop 0
	v_mfma_i32_16x16x64_i8 v[6:9], v[138:141], v[218:221], v[6:9]
	v_mfma_i32_16x16x64_i8 v[2:5], v[134:137], v[214:217], 0
	s_nop 0
	v_mfma_i32_16x16x64_i8 v[2:5], v[130:133], v[218:221], v[2:5]
	s_setprio 0
	s_barrier
	s_add_i32 s89, 0, 0x18000
	s_add_i32 s90, 0, 0x1c000
	v_add_u32_e32 v142, s89, v181
	v_add_u32_e32 v158, s90, v181
	ds_read_b128 v[130:133], v142
	ds_read_b128 v[134:137], v142 offset:1024
	ds_read_b128 v[138:141], v142 offset:2048
	ds_read_b128 v[142:145], v142 offset:3072
	ds_read_b128 v[146:149], v158
	ds_read_b128 v[150:153], v158 offset:1024
	ds_read_b128 v[154:157], v158 offset:2048
	ds_read_b128 v[158:161], v158 offset:3072
	s_add_u32 s54, s54, 0x40000
	s_addc_u32 s55, s55, 0
	s_mov_b32 m0, s68
	v_lshl_add_u64 v[222:223], s[54:55], 0, v[162:163]
	ds_read_b128 v[190:193], v189 offset:32768
	ds_read_b128 v[194:197], v189 offset:33792
	ds_read_b128 v[198:201], v189 offset:34816
	ds_read_b128 v[202:205], v189 offset:35840
	ds_read_b128 v[206:209], v189 offset:36864
	ds_read_b128 v[210:213], v189 offset:37888
	ds_read_b128 v[214:217], v189 offset:38912
	ds_read_b128 v[218:221], v189 offset:39936
	global_load_lds_dwordx4 v[222:223], off
	v_lshl_add_u64 v[222:223], s[54:55], 0, v[166:167]
	s_mov_b32 m0, s69
	s_nop 0
	global_load_lds_dwordx4 v[222:223], off
	s_waitcnt vmcnt(8)
	s_waitcnt lgkmcnt(0)
	s_barrier
	s_setprio 1
	s_waitcnt lgkmcnt(0)
	v_mfma_i32_16x16x64_i8 v[126:129], v[130:133], v[190:193], v[126:129]
	s_nop 0
	v_mfma_i32_16x16x64_i8 v[126:129], v[134:137], v[194:197], v[126:129]
	v_mfma_i32_16x16x64_i8 v[118:121], v[138:141], v[190:193], v[118:121]
	s_nop 0
	v_mfma_i32_16x16x64_i8 v[118:121], v[142:145], v[194:197], v[118:121]
	v_mfma_i32_16x16x64_i8 v[114:117], v[130:133], v[198:201], v[114:117]
	s_nop 0
	v_mfma_i32_16x16x64_i8 v[114:117], v[134:137], v[202:205], v[114:117]
	v_mfma_i32_16x16x64_i8 v[110:113], v[138:141], v[198:201], v[110:113]
	s_nop 0
	v_mfma_i32_16x16x64_i8 v[110:113], v[142:145], v[202:205], v[110:113]
	v_mfma_i32_16x16x64_i8 v[94:97], v[130:133], v[206:209], v[94:97]
	s_nop 0
	v_mfma_i32_16x16x64_i8 v[94:97], v[134:137], v[210:213], v[94:97]
	v_mfma_i32_16x16x64_i8 v[86:89], v[138:141], v[206:209], v[86:89]
	s_nop 0
	v_mfma_i32_16x16x64_i8 v[86:89], v[142:145], v[210:213], v[86:89]
	v_mfma_i32_16x16x64_i8 v[82:85], v[130:133], v[214:217], v[82:85]
	s_nop 0
	v_mfma_i32_16x16x64_i8 v[82:85], v[134:137], v[218:221], v[82:85]
	v_mfma_i32_16x16x64_i8 v[74:77], v[138:141], v[214:217], v[74:77]
	s_nop 0
	v_mfma_i32_16x16x64_i8 v[74:77], v[142:145], v[218:221], v[74:77]
	s_setprio 0
	s_setprio 1
	v_mfma_i32_16x16x64_i8 v[122:125], v[146:149], v[190:193], v[122:125]
	s_nop 0
	v_mfma_i32_16x16x64_i8 v[122:125], v[150:153], v[194:197], v[122:125]
	v_mfma_i32_16x16x64_i8 v[106:109], v[154:157], v[190:193], v[106:109]
	s_nop 0
	v_mfma_i32_16x16x64_i8 v[106:109], v[158:161], v[194:197], v[106:109]
	v_mfma_i32_16x16x64_i8 v[102:105], v[146:149], v[198:201], v[102:105]
	s_nop 0
	v_mfma_i32_16x16x64_i8 v[102:105], v[150:153], v[202:205], v[102:105]
	v_mfma_i32_16x16x64_i8 v[98:101], v[154:157], v[198:201], v[98:101]
	s_nop 0
	v_mfma_i32_16x16x64_i8 v[98:101], v[158:161], v[202:205], v[98:101]
	v_mfma_i32_16x16x64_i8 v[90:93], v[146:149], v[206:209], v[90:93]
	s_nop 0
	v_mfma_i32_16x16x64_i8 v[90:93], v[150:153], v[210:213], v[90:93]
	v_mfma_i32_16x16x64_i8 v[78:81], v[154:157], v[206:209], v[78:81]
	s_nop 0
	v_mfma_i32_16x16x64_i8 v[78:81], v[158:161], v[210:213], v[78:81]
	v_mfma_i32_16x16x64_i8 v[70:73], v[146:149], v[214:217], v[70:73]
	s_nop 0
	v_mfma_i32_16x16x64_i8 v[70:73], v[150:153], v[218:221], v[70:73]
	v_mfma_i32_16x16x64_i8 v[66:69], v[154:157], v[214:217], v[66:69]
	s_nop 0
	v_mfma_i32_16x16x64_i8 v[66:69], v[158:161], v[218:221], v[66:69]
	s_setprio 0
	s_barrier
	s_add_i32 s54, s89, s67
	v_lshl_add_u64 v[174:175], v[174:175], 0, s[28:29]
	s_mov_b32 m0, s54
	ds_read_b128 v[190:193], v189 offset:49152
	ds_read_b128 v[194:197], v189 offset:50176
	ds_read_b128 v[198:201], v189 offset:51200
	ds_read_b128 v[202:205], v189 offset:52224
	ds_read_b128 v[206:209], v189 offset:53248
	ds_read_b128 v[210:213], v189 offset:54272
	ds_read_b128 v[214:217], v189 offset:55296
	ds_read_b128 v[218:221], v189 offset:56320
	global_load_lds_dwordx4 v[174:175], off
	s_add_i32 m0, s54, 0x2000
	s_add_u32 s52, s52, 0x40080
	v_lshl_add_u64 v[174:175], v[176:177], 0, s[28:29]
	s_addc_u32 s53, s53, 0
	s_add_i32 s54, s90, s67
	global_load_lds_dwordx4 v[174:175], off
	v_lshl_add_u64 v[174:175], s[52:53], 0, v[164:165]
	s_mov_b32 m0, s54
	s_nop 0
	global_load_lds_dwordx4 v[174:175], off
	v_lshl_add_u64 v[174:175], s[52:53], 0, v[168:169]
	s_add_i32 m0, s54, 0x2000
	s_nop 0
	global_load_lds_dwordx4 v[174:175], off
	v_lshl_add_u64 v[174:175], v[182:183], 0, s[28:29]
	s_mov_b32 m0, s71
	s_nop 0
	global_load_lds_dwordx4 v[174:175], off
	v_lshl_add_u64 v[174:175], v[184:185], 0, s[28:29]
	s_mov_b32 m0, s72
	s_nop 0
	global_load_lds_dwordx4 v[174:175], off
	s_waitcnt vmcnt(8)
	s_waitcnt lgkmcnt(0)
	s_barrier
	s_setprio 1
	s_waitcnt lgkmcnt(0)
	v_mfma_i32_16x16x64_i8 v[62:65], v[130:133], v[190:193], v[62:65]
	s_nop 0
	v_mfma_i32_16x16x64_i8 v[62:65], v[134:137], v[194:197], v[62:65]
	v_mfma_i32_16x16x64_i8 v[58:61], v[138:141], v[190:193], v[58:61]
	s_nop 0
	v_mfma_i32_16x16x64_i8 v[58:61], v[142:145], v[194:197], v[58:61]
	v_mfma_i32_16x16x64_i8 v[50:53], v[130:133], v[198:201], v[50:53]
	s_nop 0
	v_mfma_i32_16x16x64_i8 v[50:53], v[134:137], v[202:205], v[50:53]
	v_mfma_i32_16x16x64_i8 v[42:45], v[138:141], v[198:201], v[42:45]
	s_nop 0
	v_mfma_i32_16x16x64_i8 v[42:45], v[142:145], v[202:205], v[42:45]
	v_mfma_i32_16x16x64_i8 v[34:37], v[130:133], v[206:209], v[34:37]
	s_nop 0
	v_mfma_i32_16x16x64_i8 v[34:37], v[134:137], v[210:213], v[34:37]
	v_mfma_i32_16x16x64_i8 v[26:29], v[138:141], v[206:209], v[26:29]
	s_nop 0
	v_mfma_i32_16x16x64_i8 v[26:29], v[142:145], v[210:213], v[26:29]
	v_mfma_i32_16x16x64_i8 v[18:21], v[130:133], v[214:217], v[18:21]
	s_nop 0
	v_mfma_i32_16x16x64_i8 v[18:21], v[134:137], v[218:221], v[18:21]
	v_mfma_i32_16x16x64_i8 v[10:13], v[138:141], v[214:217], v[10:13]
	s_nop 0
	v_mfma_i32_16x16x64_i8 v[10:13], v[142:145], v[218:221], v[10:13]
	s_setprio 0
	s_setprio 1
	v_mfma_i32_16x16x64_i8 v[54:57], v[146:149], v[190:193], v[54:57]
	s_nop 0
	v_mfma_i32_16x16x64_i8 v[54:57], v[150:153], v[194:197], v[54:57]
	v_mfma_i32_16x16x64_i8 v[46:49], v[154:157], v[190:193], v[46:49]
	s_nop 0
	v_mfma_i32_16x16x64_i8 v[46:49], v[158:161], v[194:197], v[46:49]
	v_mfma_i32_16x16x64_i8 v[38:41], v[146:149], v[198:201], v[38:41]
	s_nop 0
	v_mfma_i32_16x16x64_i8 v[38:41], v[150:153], v[202:205], v[38:41]
	v_mfma_i32_16x16x64_i8 v[30:33], v[154:157], v[198:201], v[30:33]
	s_nop 0
	v_mfma_i32_16x16x64_i8 v[30:33], v[158:161], v[202:205], v[30:33]
	v_mfma_i32_16x16x64_i8 v[22:25], v[146:149], v[206:209], v[22:25]
	s_nop 0
	v_mfma_i32_16x16x64_i8 v[22:25], v[150:153], v[210:213], v[22:25]
	v_mfma_i32_16x16x64_i8 v[14:17], v[154:157], v[206:209], v[14:17]
	s_nop 0
	v_mfma_i32_16x16x64_i8 v[14:17], v[158:161], v[210:213], v[14:17]
	v_mfma_i32_16x16x64_i8 v[6:9], v[146:149], v[214:217], v[6:9]
	s_nop 0
	v_mfma_i32_16x16x64_i8 v[6:9], v[150:153], v[218:221], v[6:9]
	v_mfma_i32_16x16x64_i8 v[2:5], v[154:157], v[214:217], v[2:5]
	s_nop 0
	v_mfma_i32_16x16x64_i8 v[2:5], v[158:161], v[218:221], v[2:5]
	s_setprio 0
	s_barrier
	s_add_i32 s88, s88, 2
	s_add_u32 s50, s50, 0x100
	s_addc_u32 s51, s51, 0
	s_add_u32 s86, s86, 0x100
	s_addc_u32 s87, s87, 0
	s_cmp_gt_u32 s88, 13
	s_cbranch_scc1 .Lpeel_exit_1723

	.amdhsa_kernel _Z8yoco_fwd4Args
		.amdhsa_group_segment_fixed_size 0
		.amdhsa_private_segment_fixed_size 0
		.amdhsa_kernarg_size 504
		.amdhsa_user_sgpr_count 2
		.amdhsa_user_sgpr_dispatch_ptr 0
		.amdhsa_user_sgpr_queue_ptr 0
		.amdhsa_user_sgpr_kernarg_segment_ptr 1
		.amdhsa_user_sgpr_dispatch_id 0
		.amdhsa_user_sgpr_kernarg_preload_length 0
		.amdhsa_user_sgpr_kernarg_preload_offset 0
		.amdhsa_user_sgpr_private_segment_size 0
		.amdhsa_uses_dynamic_stack 0
		.amdhsa_enable_private_segment 0
		.amdhsa_system_sgpr_workgroup_id_x 1
		.amdhsa_system_sgpr_workgroup_id_y 0
		.amdhsa_system_sgpr_workgroup_id_z 0
		.amdhsa_system_sgpr_workgroup_info 0
		.amdhsa_system_vgpr_workitem_id 0
		.amdhsa_next_free_vgpr 256
		.amdhsa_next_free_sgpr 101
		.amdhsa_accum_offset 256
		.amdhsa_reserve_vcc 1
		.amdhsa_float_round_mode_32 0
		.amdhsa_float_round_mode_16_64 0
		.amdhsa_float_denorm_mode_32 3
		.amdhsa_float_denorm_mode_16_64 3
		.amdhsa_dx10_clamp 1
		.amdhsa_ieee_mode 1
		.amdhsa_fp16_overflow 0
		.amdhsa_tg_split 0
		.amdhsa_exception_fp_ieee_invalid_op 0
		.amdhsa_exception_fp_denorm_src 0
		.amdhsa_exception_fp_ieee_div_zero 0
		.amdhsa_exception_fp_ieee_overflow 0
		.amdhsa_exception_fp_ieee_underflow 0
		.amdhsa_exception_fp_ieee_inexact 0
		.amdhsa_exception_int_div_zero 0
	.end_amdhsa_kernel

amdhsa.kernels:
  - .agpr_count:     0
    .args:
      - .offset:         0
        .size:           248
        .value_kind:     by_value
      - .offset:         248
        .size:           4
        .value_kind:     hidden_block_count_x
      - .offset:         252
        .size:           4
        .value_kind:     hidden_block_count_y
      - .offset:         256
        .size:           4
        .value_kind:     hidden_block_count_z
      - .offset:         260
        .size:           2
        .value_kind:     hidden_group_size_x
      - .offset:         262
        .size:           2
        .value_kind:     hidden_group_size_y
      - .offset:         264
        .size:           2
        .value_kind:     hidden_group_size_z
      - .offset:         266
        .size:           2
        .value_kind:     hidden_remainder_x
      - .offset:         268
        .size:           2
        .value_kind:     hidden_remainder_y
      - .offset:         270
        .size:           2
        .value_kind:     hidden_remainder_z
      - .offset:         288
        .size:           8
        .value_kind:     hidden_global_offset_x
      - .offset:         296
        .size:           8
        .value_kind:     hidden_global_offset_y
      - .offset:         304
        .size:           8
        .value_kind:     hidden_global_offset_z
      - .offset:         312
        .size:           2
        .value_kind:     hidden_grid_dims
      - .offset:         368
        .size:           4
        .value_kind:     hidden_dynamic_lds_size
    .group_segment_fixed_size: 0
    .kernarg_segment_align: 8
    .kernarg_segment_size: 504
    .language:       OpenCL C
    .language_version:
      - 2
      - 0
    .max_flat_workgroup_size: 512
    .name:           _Z8yoco_fwd4Args
    .private_segment_fixed_size: 0
    .sgpr_count:     107
    .sgpr_spill_count: 440
    .symbol:         _Z8yoco_fwd4Args.kd
    .uniform_work_group_size: 1
    .uses_dynamic_stack: false
    .vgpr_count:     256
    .vgpr_spill_count: 0
    .wavefront_size: 64
